# attention loop back edge tested on the scalar flag directly (no v_cndmask / v_cmp round trip through a VGPR)
# speedup vs baseline: 1.0117x; 1.0090x over previous
.LBB0_481:
.LBB0_483:
	s_andn2_b64 vcc, exec, s[96:97]
	v_cvt_pk_bf16_f32 v72, v41, v46
	v_cvt_pk_bf16_f32 v73, v47, v53
	v_cvt_pk_bf16_f32 v74, v54, v67
	v_cvt_pk_bf16_f32 v75, v68, v69
	s_waitcnt lgkmcnt(0)
	ds_read_b64_tr_b16 v[236:237], v201 offset:8192
	ds_read_b64_tr_b16 v[238:239], v201 offset:9216
	ds_read_b64_tr_b16 v[240:241], v202 offset:8192
	ds_read_b64_tr_b16 v[242:243], v202 offset:9216
	v_cvt_pk_bf16_f32 v44, v38, v44
	v_cvt_pk_bf16_f32 v45, v45, v51
	v_cvt_pk_bf16_f32 v46, v52, v57
	v_cvt_pk_bf16_f32 v47, v58, v62
	s_nop 0
	v_mfma_f32_32x32x16_bf16 v[18:33], v[228:231], v[72:75], v[18:33]
	v_mfma_f32_32x32x16_bf16 v[2:17], v[232:235], v[72:75], v[2:17]
	s_waitcnt lgkmcnt(0)
	ds_read_b64_tr_b16 v[228:229], v195 offset:16384
	ds_read_b64_tr_b16 v[230:231], v195 offset:17408
	ds_read_b64_tr_b16 v[232:233], v196 offset:16384
	ds_read_b64_tr_b16 v[234:235], v196 offset:17408
	v_cvt_pk_bf16_f32 v42, v37, v42
	v_cvt_pk_bf16_f32 v43, v43, v49
	s_nop 0
	v_mfma_f32_32x32x16_bf16 v[18:33], v[236:239], v[44:47], v[18:33]
	v_mfma_f32_32x32x16_bf16 v[2:17], v[240:243], v[44:47], v[2:17]
	v_cvt_pk_bf16_f32 v44, v50, v55
	v_cvt_pk_bf16_f32 v45, v56, v61
	s_waitcnt lgkmcnt(0)
	ds_read_b64_tr_b16 v[236:237], v197 offset:16384
	ds_read_b64_tr_b16 v[238:239], v197 offset:17408
	ds_read_b64_tr_b16 v[240:241], v198 offset:16384
	ds_read_b64_tr_b16 v[242:243], v198 offset:17408
	v_cvt_pk_bf16_f32 v34, v36, v39
	v_cvt_pk_bf16_f32 v35, v40, v48
	v_cvt_pk_bf16_f32 v36, v63, v65
	v_cvt_pk_bf16_f32 v37, v64, v70
	s_nop 0
	v_mfma_f32_32x32x16_bf16 v[18:33], v[228:231], v[42:45], v[18:33]
	v_mfma_f32_32x32x16_bf16 v[2:17], v[232:235], v[42:45], v[2:17]
	s_waitcnt lgkmcnt(0)
	s_nop 0
	v_mfma_f32_32x32x16_bf16 v[18:33], v[236:239], v[34:37], v[18:33]
	v_mfma_f32_32x32x16_bf16 v[2:17], v[240:243], v[34:37], v[2:17]
	s_cbranch_vccnz .LBB0_485
	s_waitcnt vmcnt(0)

.LBB0_487:
	s_or_b64 exec, exec, s[4:5]
	s_waitcnt lgkmcnt(0)
	s_andn2_b64 vcc, exec, s[96:97]
	s_cbranch_vccnz .LBB0_430
	v_mov_b64_e32 v[146:147], v[174:175]
	v_mov_b64_e32 v[150:151], v[170:171]
	v_mov_b64_e32 v[154:155], v[166:167]
	v_mov_b64_e32 v[158:159], v[162:163]
	v_mov_b64_e32 v[148:149], v[176:177]
	v_mov_b64_e32 v[152:153], v[172:173]
	v_mov_b64_e32 v[156:157], v[168:169]
	v_mov_b64_e32 v[160:161], v[164:165]
	v_mov_b32_e32 v182, v187
	v_mov_b32_e32 v178, v190
	v_mov_b32_e32 v180, v183
	s_mov_b32 s82, s48
	s_mov_b32 s42, s80
	s_mov_b32 s33, s41
	s_mov_b32 s81, s47
	s_mov_b32 s88, s40
	s_mov_b32 s86, s39
	s_lshl_b32 s4, s88, 7
	v_add_u32_e32 v2, s4, v248
	s_lshl_b32 s5, s81, 3
	v_mul_u32_u24_e32 v3, s81, v249
	v_add_u32_e32 v3, s82, v3
	v_max_i32_e32 v4, 0, v3
	s_mov_b32 m0, s24
	v_mad_u32_u24 v5, v4, s21, v2
	global_load_lds_dwordx4 v5, s[84:85]
	v_add_u32_e32 v3, s5, v3
	v_max_i32_e32 v4, 0, v3
	s_add_u32 m0, s24, 0x400
	v_mad_u32_u24 v5, v4, s21, v2
	global_load_lds_dwordx4 v5, s[84:85]
	v_add_u32_e32 v3, s5, v3
	v_max_i32_e32 v4, 0, v3
	s_add_u32 m0, s24, 0x800
	v_mad_u32_u24 v5, v4, s21, v2
	global_load_lds_dwordx4 v5, s[84:85]
	v_add_u32_e32 v3, s5, v3
	v_max_i32_e32 v4, 0, v3
	s_add_u32 m0, s24, 0xc00
	v_mad_u32_u24 v5, v4, s21, v2
	global_load_lds_dwordx4 v5, s[84:85]
	v_mul_u32_u24_e32 v3, s81, v250
	v_add_u32_e32 v3, s82, v3
	v_max_i32_e32 v4, 0, v3
	s_mov_b32 m0, s26
	v_mad_u32_u24 v5, v4, s21, v2
	global_load_lds_dwordx4 v5, s[84:85]
	v_add_u32_e32 v3, s5, v3
	v_max_i32_e32 v4, 0, v3
	s_add_u32 m0, s26, 0x400
	v_mad_u32_u24 v5, v4, s21, v2
	global_load_lds_dwordx4 v5, s[84:85]
	v_add_u32_e32 v3, s5, v3
	v_max_i32_e32 v4, 0, v3
	s_add_u32 m0, s26, 0x800
	v_mad_u32_u24 v5, v4, s21, v2
	global_load_lds_dwordx4 v5, s[84:85]
	v_add_u32_e32 v3, s5, v3
	v_max_i32_e32 v4, 0, v3
	s_add_u32 m0, s26, 0xc00
	v_mad_u32_u24 v5, v4, s21, v2
	global_load_lds_dwordx4 v5, s[84:85]
	s_branch .LBB0_430
